# speedup vs baseline: 1.0064x; 1.0064x over previous
_Z13gather_kernelPK15HIP_vector_typeIjLj2EEPKiPK6OvfRecPKDF16_PKfPDF16_:
	s_lshr_b32 s3, s2, 2
	s_and_b32 s3, s3, 0x3ffffffe
	s_and_b32 s4, s2, 1
	s_or_b32 s3, s3, s4
	s_cmpk_gt_u32 s3, 0x186
	s_cbranch_scc1 .LBB1_156
	s_load_dwordx4 s[8:11], s[0:1], 0x0
	s_movk_i32 s4, 0x80
	s_lshl_b32 s12, s3, 4
	s_addk_i32 s12, 0x800
	v_lshrrev_b32_e32 v2, 6, v0
	v_cmp_gt_u32_e64 s[4:5], s4, v0
	v_lshlrev_b32_e32 v1, 2, v0
	v_readfirstlane_b32 s62, v2
	s_and_saveexec_b64 s[6:7], s[4:5]
	v_mov_b32_e32 v2, 0
	ds_write_b32 v1, v2 offset:10832
	s_or_b64 exec, exec, s[6:7]
	s_waitcnt lgkmcnt(0)
	v_cmp_gt_u32_e64 s[6:7], 64, v0
	s_and_saveexec_b64 s[12:13], s[6:7]
	v_mov_b32_e32 v2, 0
	ds_write_b32 v1, v2 offset:11856
	s_or_b64 exec, exec, s[12:13]
	s_waitcnt lgkmcnt(0)
	s_mul_i32 s15, s3, 0x5000
	s_mul_hi_u32 s13, s3, 0x5000
	s_add_u32 s8, s8, s15
	s_addc_u32 s9, s9, s13
	v_lshlrev_b32_e32 v2, 3, v0
	v_mov_b32_e32 v3, 0
	v_lshl_add_u64 v[4:5], s[8:9], 0, v[2:3]
	s_movk_i32 s13, 0x1000
	global_load_dwordx2 v[20:21], v2, s[8:9]
	global_load_dwordx2 v[18:19], v2, s[8:9] offset:2048
	v_add_co_u32_e32 v2, vcc, s13, v4
	s_movk_i32 s13, 0x2000
	s_nop 0
	v_addc_co_u32_e32 v3, vcc, 0, v5, vcc
	v_add_co_u32_e32 v6, vcc, s13, v4
	s_movk_i32 s13, 0x3000
	s_nop 0
	v_addc_co_u32_e32 v7, vcc, 0, v5, vcc
	v_add_co_u32_e32 v24, vcc, s13, v4
	v_or_b32_e32 v23, 0x400, v0
	s_nop 0
	v_addc_co_u32_e32 v25, vcc, 0, v5, vcc
	v_lshlrev_b32_e32 v8, 3, v23
	v_or_b32_e32 v22, 0x800, v0
	v_add_co_u32_e32 v26, vcc, 0x4000, v4
	global_load_dwordx2 v[16:17], v[2:3], off
	global_load_dwordx2 v[14:15], v[2:3], off offset:2048
	global_load_dwordx2 v[12:13], v8, s[8:9]
	global_load_dwordx2 v[10:11], v[6:7], off offset:2048
	v_lshlrev_b32_e32 v28, 3, v22
	v_addc_co_u32_e32 v27, vcc, 0, v5, vcc
	global_load_dwordx2 v[8:9], v[24:25], off
	global_load_dwordx2 v[6:7], v[24:25], off offset:2048
	global_load_dwordx2 v[4:5], v28, s[8:9]
	global_load_dwordx2 v[2:3], v[26:27], off offset:2048
	s_lshl_b32 s51, s3, 4
	s_addk_i32 s51, 0x800
	s_load_dwordx4 s[36:39], s[10:11], s51 offset:0x0
	v_mov_b32_e32 v54, 1
	s_waitcnt lgkmcnt(0)
	s_barrier
	s_min_u32 s36, s36, 0x280
	s_min_u32 s37, s37, 0x280
	s_min_u32 s38, s38, 0x280
	s_min_u32 s39, s39, 0x280
	s_addk_i32 s37, 0x280
	s_addk_i32 s38, 0x500
	s_addk_i32 s39, 0x780
	s_cmp_ge_u32 s62, 2
	s_cselect_b32 s54, s37, s36
	s_cselect_b32 s59, s39, s38
	s_mov_b32 s52, s36
	s_mov_b32 s53, s36
	s_mov_b32 s55, s37
	s_mov_b32 s56, s37
	s_mov_b32 s57, s38
	s_mov_b32 s58, s38
	s_mov_b32 s60, s39
	s_mov_b32 s61, s39
	v_cmp_gt_i32_e32 vcc, s52, v0
	s_and_saveexec_b64 s[8:9], vcc
	s_waitcnt vmcnt(9)
	v_lshrrev_b32_e32 v33, 16, v20
	v_lshlrev_b32_e32 v53, 2, v33
	ds_add_rtn_u32 v43, v53, v54 offset:10832
	s_or_b64 exec, exec, s[8:9]
	v_or_b32_e32 v55, 0x100, v0
	v_cmp_gt_i32_e32 vcc, s53, v55
	s_and_saveexec_b64 s[8:9], vcc
	s_waitcnt vmcnt(8)
	v_lshrrev_b32_e32 v34, 16, v18
	v_lshlrev_b32_e32 v53, 2, v34
	ds_add_rtn_u32 v44, v53, v54 offset:10832
	s_or_b64 exec, exec, s[8:9]
	v_or_b32_e32 v55, 0x200, v0
	v_cmp_gt_i32_e32 vcc, s54, v55
	s_and_saveexec_b64 s[8:9], vcc
	s_waitcnt vmcnt(7)
	v_lshrrev_b32_e32 v35, 16, v16
	v_lshlrev_b32_e32 v53, 2, v35
	ds_add_rtn_u32 v45, v53, v54 offset:10832
	s_or_b64 exec, exec, s[8:9]
	v_or_b32_e32 v55, 0x300, v0
	v_cmp_gt_i32_e32 vcc, s55, v55
	s_and_saveexec_b64 s[8:9], vcc
	s_waitcnt vmcnt(6)
	v_lshrrev_b32_e32 v36, 16, v14
	v_lshlrev_b32_e32 v53, 2, v36
	ds_add_rtn_u32 v46, v53, v54 offset:10832
	s_or_b64 exec, exec, s[8:9]
	v_or_b32_e32 v55, 0x400, v0
	v_cmp_gt_i32_e32 vcc, s56, v55
	s_and_saveexec_b64 s[8:9], vcc
	s_waitcnt vmcnt(5)
	v_lshrrev_b32_e32 v37, 16, v12
	v_lshlrev_b32_e32 v53, 2, v37
	ds_add_rtn_u32 v47, v53, v54 offset:10832
	s_or_b64 exec, exec, s[8:9]
	v_or_b32_e32 v55, 0x500, v0
	v_cmp_gt_i32_e32 vcc, s57, v55
	s_and_saveexec_b64 s[8:9], vcc
	s_waitcnt vmcnt(4)
	v_lshrrev_b32_e32 v38, 16, v10
	v_lshlrev_b32_e32 v53, 2, v38
	ds_add_rtn_u32 v48, v53, v54 offset:10832
	s_or_b64 exec, exec, s[8:9]
	v_or_b32_e32 v55, 0x600, v0
	v_cmp_gt_i32_e32 vcc, s58, v55
	s_and_saveexec_b64 s[8:9], vcc
	s_waitcnt vmcnt(3)
	v_lshrrev_b32_e32 v39, 16, v8
	v_lshlrev_b32_e32 v53, 2, v39
	ds_add_rtn_u32 v49, v53, v54 offset:10832
	s_or_b64 exec, exec, s[8:9]
	v_or_b32_e32 v55, 0x700, v0
	v_cmp_gt_i32_e32 vcc, s59, v55
	s_and_saveexec_b64 s[8:9], vcc
	s_waitcnt vmcnt(2)
	v_lshrrev_b32_e32 v40, 16, v6
	v_lshlrev_b32_e32 v53, 2, v40
	ds_add_rtn_u32 v50, v53, v54 offset:10832
	s_or_b64 exec, exec, s[8:9]
	v_or_b32_e32 v55, 0x800, v0
	v_cmp_gt_i32_e32 vcc, s60, v55
	s_and_saveexec_b64 s[8:9], vcc
	s_waitcnt vmcnt(1)
	v_lshrrev_b32_e32 v41, 16, v4
	v_lshlrev_b32_e32 v53, 2, v41
	ds_add_rtn_u32 v51, v53, v54 offset:10832
	s_or_b64 exec, exec, s[8:9]
	v_or_b32_e32 v55, 0x900, v0
	v_cmp_gt_i32_e32 vcc, s61, v55
	s_and_saveexec_b64 s[8:9], vcc
	s_waitcnt vmcnt(0)
	v_lshrrev_b32_e32 v42, 16, v2
	v_lshlrev_b32_e32 v53, 2, v42
	ds_add_rtn_u32 v52, v53, v54 offset:10832
	s_or_b64 exec, exec, s[8:9]
	s_waitcnt lgkmcnt(0)
	v_cmp_gt_i32_e32 vcc, s52, v0
	v_lshl_or_b32 v56, v43, 8, v33
	s_nop 0
	v_cndmask_b32_e32 v32, -1, v56, vcc
	v_or_b32_e32 v55, 0x100, v0
	v_cmp_gt_i32_e32 vcc, s53, v55
	v_lshl_or_b32 v56, v44, 8, v34
	s_nop 0
	v_cndmask_b32_e32 v27, -1, v56, vcc
	v_or_b32_e32 v55, 0x200, v0
	v_cmp_gt_i32_e32 vcc, s54, v55
	v_lshl_or_b32 v56, v45, 8, v35
	s_nop 0
	v_cndmask_b32_e32 v31, -1, v56, vcc
	v_or_b32_e32 v55, 0x300, v0
	v_cmp_gt_i32_e32 vcc, s55, v55
	v_lshl_or_b32 v56, v46, 8, v36
	s_nop 0
	v_cndmask_b32_e32 v26, -1, v56, vcc
	v_or_b32_e32 v55, 0x400, v0
	v_cmp_gt_i32_e32 vcc, s56, v55
	v_lshl_or_b32 v56, v47, 8, v37
	s_nop 0
	v_cndmask_b32_e32 v30, -1, v56, vcc
	v_or_b32_e32 v55, 0x500, v0
	v_cmp_gt_i32_e32 vcc, s57, v55
	v_lshl_or_b32 v56, v48, 8, v38
	s_nop 0
	v_cndmask_b32_e32 v24, -1, v56, vcc
	v_or_b32_e32 v55, 0x600, v0
	v_cmp_gt_i32_e32 vcc, s58, v55
	v_lshl_or_b32 v56, v49, 8, v39
	s_nop 0
	v_cndmask_b32_e32 v29, -1, v56, vcc
	v_or_b32_e32 v55, 0x700, v0
	v_cmp_gt_i32_e32 vcc, s59, v55
	v_lshl_or_b32 v56, v50, 8, v40
	s_nop 0
	v_cndmask_b32_e32 v23, -1, v56, vcc
	v_or_b32_e32 v55, 0x800, v0
	v_cmp_gt_i32_e32 vcc, s60, v55
	v_lshl_or_b32 v56, v51, 8, v41
	s_nop 0
	v_cndmask_b32_e32 v28, -1, v56, vcc
	v_or_b32_e32 v55, 0x900, v0
	v_cmp_gt_i32_e32 vcc, s61, v55
	v_lshl_or_b32 v56, v52, 8, v42
	s_nop 0
	v_cndmask_b32_e32 v22, -1, v56, vcc
